# baseline (speedup 1.0000x reference)
_Z11edge_kernelILi36ELb1EEvPKfS1_PKDF16_PKiS5_S1_S1_S1_S1_S1_PDF16_:
	s_load_dwordx8 s[4:11], s[0:1], 0x0
	s_load_dwordx8 s[12:19], s[0:1], 0x20
	s_load_dwordx4 s[20:23], s[0:1], 0x40
	s_load_dwordx2 s[24:25], s[0:1], 0x50
	v_readfirstlane_b32 s3, v0
	v_bfe_u32 v75, v0, 4, 2
	v_and_b32_e32 v76, 15, v0
	v_and_b32_e32 v78, 63, v0
	s_lshr_b32 s3, s3, 6
	s_lshl_b32 s2, s2, 1
	s_add_i32 s2, s2, s3
	v_lshlrev_b32_e32 v74, 8, v75
	v_lshl_or_b32 v74, v76, 4, v74
	v_lshlrev_b32_e32 v79, 4, v78
	v_lshl_or_b32 v77, v76, 2, v75
	v_lshlrev_b32_e32 v77, 2, v77
	v_mul_u32_u24_e32 v73, 0x900, v75
	v_lshl_or_b32 v73, v76, 4, v73
	v_mul_u32_u24_e32 v78, 36, v75
	s_mul_i32 s28, s2, 0x2400
	s_lshl_b32 s29, s2, 14
	s_lshl_b32 s30, s2, 2
	s_lshl_b32 s31, s2, 8
	s_lshl_b32 s33, s3, 10
	s_lshl_b32 s34, s3, 8
	s_addk_i32 s34, 0x4000
	s_waitcnt lgkmcnt(0)
	s_add_u32 s10, s10, s30
	s_addc_u32 s11, s11, 0
	s_add_u32 s12, s12, s30
	s_addc_u32 s13, s13, 0
	s_load_dword s35, s[10:11], 0x0
	s_load_dword s36, s[12:13], 0x0
	s_add_u32 s14, s14, s28
	s_addc_u32 s15, s15, 0
	global_load_dwordx4 v[0:3], v73, s[14:15] nt
	global_load_dwordx4 v[4:7], v73, s[14:15] offset:256 nt
	global_load_dwordx4 v[8:11], v73, s[14:15] offset:512 nt
	global_load_dwordx4 v[12:15], v73, s[14:15] offset:768 nt
	global_load_dwordx4 v[16:19], v73, s[14:15] offset:1024 nt
	global_load_dwordx4 v[20:23], v73, s[14:15] offset:1280 nt
	global_load_dwordx4 v[24:27], v73, s[14:15] offset:1536 nt
	global_load_dwordx4 v[28:31], v73, s[14:15] offset:1792 nt
	global_load_dwordx4 v[32:35], v73, s[14:15] offset:2048 nt
	s_add_u32 s22, s22, s33
	s_addc_u32 s23, s23, 0
	s_add_u32 s18, s18, s29
	s_addc_u32 s19, s19, 0
	s_mov_b32 m0, s33
	s_nop 0
	global_load_lds_dwordx4 v79, s[22:23]
	global_load_lds_dwordx4 v79, s[22:23] offset:2048
	s_add_u32 m0, m0, 0x1000
	s_add_u32 s22, s22, 0x1000
	s_addc_u32 s23, s23, 0
	global_load_lds_dwordx4 v79, s[22:23]
	global_load_lds_dwordx4 v79, s[22:23] offset:2048
	s_add_u32 m0, m0, 0x1000
	s_add_u32 s22, s22, 0x1000
	s_addc_u32 s23, s23, 0
	global_load_lds_dwordx4 v79, s[22:23]
	global_load_lds_dwordx4 v79, s[22:23] offset:2048
	s_add_u32 m0, m0, 0x1000
	s_add_u32 s22, s22, 0x1000
	s_addc_u32 s23, s23, 0
	global_load_lds_dwordx4 v79, s[22:23]
	global_load_lds_dwordx4 v79, s[22:23] offset:2048
	s_add_u32 s16, s16, s31
	s_addc_u32 s17, s17, 0
	s_add_u32 s20, s20, s31
	s_addc_u32 s21, s21, 0
	s_waitcnt lgkmcnt(0)
	s_lshl_b32 s36, s36, 7
	s_add_u32 s24, s24, s36
	s_addc_u32 s25, s25, 0
	s_lshl_b32 s37, s35, 7
	s_lshl_b32 s38, s35, 4
	s_add_u32 s4, s4, s37
	s_addc_u32 s5, s5, 0
	s_add_u32 s6, s6, s38
	s_addc_u32 s7, s7, 0
	v_mov_b32_e32 v93, 0
	v_mov_b32_e32 v92, v78
	v_lshl_add_u64 v[94:95], s[4:5], 0, v[92:93]
	v_lshl_add_u64 v[94:95], v[94:95], 0, 20
	v_cmp_eq_u32_e32 vcc, 3, v75
	s_nop 1
	v_mov_b32_e32 v90, s6
	v_mov_b32_e32 v91, s7
	v_cndmask_b32_e32 v94, v94, v90, vcc
	v_cndmask_b32_e32 v95, v95, v91, vcc
	global_load_dwordx4 v[80:83], v78, s[4:5] nt
	global_load_dword v84, v78, s[4:5] offset:16 nt
	global_load_dwordx4 v[86:89], v[94:95], off nt
	global_load_dword v72, v77, s[16:17] nt
	global_load_dword v64, v77, s[20:21] nt
	v_add_u32_e32 v78, s34, v77
	v_lshl_add_u32 v79, v75, 2, s34
	s_waitcnt vmcnt(2)
	s_barrier
	v_pk_mul_f32 v[96:97], v[80:81], v[0:1] op_sel_hi:[0,1]
	v_pk_mul_f32 v[98:99], v[80:81], v[2:3] op_sel_hi:[0,1]
	v_pk_mul_f32 v[100:101], v[80:81], v[4:5] op_sel:[1,0]
	v_pk_mul_f32 v[102:103], v[80:81], v[6:7] op_sel:[1,0]
	v_pk_fma_f32 v[96:97], v[82:83], v[8:9], v[96:97] op_sel_hi:[0,1,1]
	v_pk_fma_f32 v[98:99], v[82:83], v[10:11], v[98:99] op_sel_hi:[0,1,1]
	v_pk_fma_f32 v[100:101], v[82:83], v[12:13], v[100:101] op_sel:[1,0,0]
	v_pk_fma_f32 v[102:103], v[82:83], v[14:15], v[102:103] op_sel:[1,0,0]
	v_pk_fma_f32 v[96:97], v[84:85], v[16:17], v[96:97] op_sel_hi:[0,1,1]
	v_pk_fma_f32 v[98:99], v[84:85], v[18:19], v[98:99] op_sel_hi:[0,1,1]
	v_pk_fma_f32 v[100:101], v[86:87], v[20:21], v[100:101] op_sel_hi:[0,1,1]
	v_pk_fma_f32 v[102:103], v[86:87], v[22:23], v[102:103] op_sel_hi:[0,1,1]
	v_pk_fma_f32 v[96:97], v[86:87], v[24:25], v[96:97] op_sel:[1,0,0]
	v_pk_fma_f32 v[98:99], v[86:87], v[26:27], v[98:99] op_sel:[1,0,0]
	v_pk_fma_f32 v[100:101], v[88:89], v[28:29], v[100:101] op_sel_hi:[0,1,1]
	v_pk_fma_f32 v[102:103], v[88:89], v[30:31], v[102:103] op_sel_hi:[0,1,1]
	v_pk_fma_f32 v[96:97], v[88:89], v[32:33], v[96:97] op_sel:[1,0,0]
	v_pk_fma_f32 v[98:99], v[88:89], v[34:35], v[98:99] op_sel:[1,0,0]
	v_pk_add_f32 v[96:97], v[96:97], v[100:101]
	v_pk_add_f32 v[98:99], v[98:99], v[102:103]
	s_nop 1
	v_permlane16_swap_b32_e32 v96, v97
	v_permlane16_swap_b32_e32 v98, v99
	v_add_f32_e32 v96, v96, v97
	v_add_f32_e32 v98, v98, v99
	s_nop 1
	v_permlane32_swap_b32_e32 v96, v98
	v_add_f32_e32 v96, v96, v98
	s_waitcnt vmcnt(1)
	v_add_f32_e32 v96, v96, v72
	v_max_f32_e32 v96, 0, v96
	ds_write_b32 v78, v96
	ds_read2_b32 v[80:81], v79 offset0:0 offset1:4
	ds_read2_b32 v[82:83], v79 offset0:8 offset1:12
	ds_read2_b32 v[84:85], v79 offset0:16 offset1:20
	ds_read2_b32 v[86:87], v79 offset0:24 offset1:28
	ds_read2_b32 v[88:89], v79 offset0:32 offset1:36
	ds_read2_b32 v[90:91], v79 offset0:40 offset1:44
	ds_read2_b32 v[92:93], v79 offset0:48 offset1:52
	ds_read2_b32 v[94:95], v79 offset0:56 offset1:60
	s_waitcnt lgkmcnt(0)
	v_cmp_neq_f32_e64 s[40:41], 0, v80
	v_cmp_neq_f32_e64 s[42:43], 0, v81
	v_cmp_neq_f32_e64 s[44:45], 0, v82
	v_cmp_neq_f32_e64 s[46:47], 0, v83
	v_cmp_neq_f32_e64 s[48:49], 0, v84
	v_cmp_neq_f32_e64 s[50:51], 0, v85
	v_cmp_neq_f32_e64 s[52:53], 0, v86
	v_cmp_neq_f32_e64 s[54:55], 0, v87
	v_cmp_neq_f32_e64 s[56:57], 0, v88
	v_cmp_neq_f32_e64 s[58:59], 0, v89
	v_cmp_neq_f32_e64 s[60:61], 0, v90
	v_cmp_neq_f32_e64 s[62:63], 0, v91
	v_cmp_neq_f32_e64 s[64:65], 0, v92
	v_cmp_neq_f32_e64 s[66:67], 0, v93
	v_cmp_neq_f32_e64 s[68:69], 0, v94
	v_cmp_neq_f32_e64 s[70:71], 0, v95
	s_mov_b64 exec, s[40:41]
	global_load_dwordx4 v[0:3], v74, s[18:19] nt
	s_mov_b64 exec, s[42:43]
	global_load_dwordx4 v[4:7], v74, s[18:19] offset:1024 nt
	s_mov_b64 exec, s[44:45]
	global_load_dwordx4 v[8:11], v74, s[18:19] offset:2048 nt
	s_mov_b64 exec, s[46:47]
	global_load_dwordx4 v[12:15], v74, s[18:19] offset:3072 nt
	s_add_u32 s18, s18, 0x1000
	s_addc_u32 s19, s19, 0
	s_mov_b64 exec, s[48:49]
	global_load_dwordx4 v[16:19], v74, s[18:19] nt
	s_mov_b64 exec, s[50:51]
	global_load_dwordx4 v[20:23], v74, s[18:19] offset:1024 nt
	s_mov_b64 exec, s[52:53]
	global_load_dwordx4 v[24:27], v74, s[18:19] offset:2048 nt
	s_mov_b64 exec, s[54:55]
	global_load_dwordx4 v[28:31], v74, s[18:19] offset:3072 nt
	s_add_u32 s18, s18, 0x1000
	s_addc_u32 s19, s19, 0
	s_mov_b64 exec, s[56:57]
	global_load_dwordx4 v[32:35], v74, s[18:19] nt
	s_mov_b64 exec, s[58:59]
	global_load_dwordx4 v[36:39], v74, s[18:19] offset:1024 nt
	s_mov_b64 exec, s[60:61]
	global_load_dwordx4 v[40:43], v74, s[18:19] offset:2048 nt
	s_mov_b64 exec, s[62:63]
	global_load_dwordx4 v[44:47], v74, s[18:19] offset:3072 nt
	s_add_u32 s18, s18, 0x1000
	s_addc_u32 s19, s19, 0
	s_mov_b64 exec, s[64:65]
	global_load_dwordx4 v[48:51], v74, s[18:19] nt
	s_mov_b64 exec, s[66:67]
	global_load_dwordx4 v[52:55], v74, s[18:19] offset:1024 nt
	s_mov_b64 exec, s[68:69]
	global_load_dwordx4 v[56:59], v74, s[18:19] offset:2048 nt
	s_mov_b64 exec, s[70:71]
	global_load_dwordx4 v[60:63], v74, s[18:19] offset:3072 nt
	s_mov_b64 exec, -1
	v_mov_b32_e32 v96, 0
	v_mov_b32_e32 v97, 0
	v_mov_b32_e32 v98, 0
	v_mov_b32_e32 v99, 0
	v_mov_b32_e32 v100, 0
	v_mov_b32_e32 v101, 0
	v_mov_b32_e32 v102, 0
	v_mov_b32_e32 v103, 0
	s_waitcnt vmcnt(12)
	s_mov_b64 exec, s[40:41]
	v_pk_fma_f32 v[96:97], v[80:81], v[0:1], v[96:97] op_sel_hi:[0,1,1]
	v_pk_fma_f32 v[98:99], v[80:81], v[2:3], v[98:99] op_sel_hi:[0,1,1]
	s_mov_b64 exec, s[42:43]
	v_pk_fma_f32 v[100:101], v[80:81], v[4:5], v[100:101] op_sel:[1,0,0]
	v_pk_fma_f32 v[102:103], v[80:81], v[6:7], v[102:103] op_sel:[1,0,0]
	s_mov_b64 exec, s[44:45]
	v_pk_fma_f32 v[96:97], v[82:83], v[8:9], v[96:97] op_sel_hi:[0,1,1]
	v_pk_fma_f32 v[98:99], v[82:83], v[10:11], v[98:99] op_sel_hi:[0,1,1]
	s_mov_b64 exec, s[46:47]
	v_pk_fma_f32 v[100:101], v[82:83], v[12:13], v[100:101] op_sel:[1,0,0]
	v_pk_fma_f32 v[102:103], v[82:83], v[14:15], v[102:103] op_sel:[1,0,0]
	s_waitcnt vmcnt(8)
	s_mov_b64 exec, s[48:49]
	v_pk_fma_f32 v[96:97], v[84:85], v[16:17], v[96:97] op_sel_hi:[0,1,1]
	v_pk_fma_f32 v[98:99], v[84:85], v[18:19], v[98:99] op_sel_hi:[0,1,1]
	s_mov_b64 exec, s[50:51]
	v_pk_fma_f32 v[100:101], v[84:85], v[20:21], v[100:101] op_sel:[1,0,0]
	v_pk_fma_f32 v[102:103], v[84:85], v[22:23], v[102:103] op_sel:[1,0,0]
	s_mov_b64 exec, s[52:53]
	v_pk_fma_f32 v[96:97], v[86:87], v[24:25], v[96:97] op_sel_hi:[0,1,1]
	v_pk_fma_f32 v[98:99], v[86:87], v[26:27], v[98:99] op_sel_hi:[0,1,1]
	s_mov_b64 exec, s[54:55]
	v_pk_fma_f32 v[100:101], v[86:87], v[28:29], v[100:101] op_sel:[1,0,0]
	v_pk_fma_f32 v[102:103], v[86:87], v[30:31], v[102:103] op_sel:[1,0,0]
	s_waitcnt vmcnt(4)
	s_mov_b64 exec, s[56:57]
	v_pk_fma_f32 v[96:97], v[88:89], v[32:33], v[96:97] op_sel_hi:[0,1,1]
	v_pk_fma_f32 v[98:99], v[88:89], v[34:35], v[98:99] op_sel_hi:[0,1,1]
	s_mov_b64 exec, s[58:59]
	v_pk_fma_f32 v[100:101], v[88:89], v[36:37], v[100:101] op_sel:[1,0,0]
	v_pk_fma_f32 v[102:103], v[88:89], v[38:39], v[102:103] op_sel:[1,0,0]
	s_mov_b64 exec, s[60:61]
	v_pk_fma_f32 v[96:97], v[90:91], v[40:41], v[96:97] op_sel_hi:[0,1,1]
	v_pk_fma_f32 v[98:99], v[90:91], v[42:43], v[98:99] op_sel_hi:[0,1,1]
	s_mov_b64 exec, s[62:63]
	v_pk_fma_f32 v[100:101], v[90:91], v[44:45], v[100:101] op_sel:[1,0,0]
	v_pk_fma_f32 v[102:103], v[90:91], v[46:47], v[102:103] op_sel:[1,0,0]
	s_waitcnt vmcnt(0)
	s_mov_b64 exec, s[64:65]
	v_pk_fma_f32 v[96:97], v[92:93], v[48:49], v[96:97] op_sel_hi:[0,1,1]
	v_pk_fma_f32 v[98:99], v[92:93], v[50:51], v[98:99] op_sel_hi:[0,1,1]
	s_mov_b64 exec, s[66:67]
	v_pk_fma_f32 v[100:101], v[92:93], v[52:53], v[100:101] op_sel:[1,0,0]
	v_pk_fma_f32 v[102:103], v[92:93], v[54:55], v[102:103] op_sel:[1,0,0]
	s_mov_b64 exec, s[68:69]
	v_pk_fma_f32 v[96:97], v[94:95], v[56:57], v[96:97] op_sel_hi:[0,1,1]
	v_pk_fma_f32 v[98:99], v[94:95], v[58:59], v[98:99] op_sel_hi:[0,1,1]
	s_mov_b64 exec, s[70:71]
	v_pk_fma_f32 v[100:101], v[94:95], v[60:61], v[100:101] op_sel:[1,0,0]
	v_pk_fma_f32 v[102:103], v[94:95], v[62:63], v[102:103] op_sel:[1,0,0]
	s_mov_b64 exec, -1
	ds_read_b128 v[0:3], v74
	ds_read_b128 v[4:7], v74 offset:1024
	ds_read_b128 v[8:11], v74 offset:2048
	ds_read_b128 v[12:15], v74 offset:3072
	ds_read_b128 v[16:19], v74 offset:4096
	ds_read_b128 v[20:23], v74 offset:5120
	ds_read_b128 v[24:27], v74 offset:6144
	ds_read_b128 v[28:31], v74 offset:7168
	ds_read_b128 v[32:35], v74 offset:8192
	ds_read_b128 v[36:39], v74 offset:9216
	ds_read_b128 v[40:43], v74 offset:10240
	ds_read_b128 v[44:47], v74 offset:11264
	ds_read_b128 v[48:51], v74 offset:12288
	ds_read_b128 v[52:55], v74 offset:13312
	ds_read_b128 v[56:59], v74 offset:14336
	v_pk_add_f32 v[96:97], v[96:97], v[100:101]
	v_pk_add_f32 v[98:99], v[98:99], v[102:103]
	s_nop 1
	v_permlane16_swap_b32_e32 v96, v97
	v_permlane16_swap_b32_e32 v98, v99
	v_add_f32_e32 v96, v96, v97
	v_add_f32_e32 v98, v98, v99
	s_nop 1
	v_permlane32_swap_b32_e32 v96, v98
	v_add_f32_e32 v96, v96, v98
	v_add_f32_e32 v96, v96, v64
	s_waitcnt lgkmcnt(5)
	ds_read_b128 v[60:63], v74 offset:15360
	ds_write_b32 v78, v96
	ds_read2_b32 v[80:81], v79 offset0:0 offset1:4
	ds_read2_b32 v[82:83], v79 offset0:8 offset1:12
	ds_read2_b32 v[84:85], v79 offset0:16 offset1:20
	ds_read2_b32 v[86:87], v79 offset0:24 offset1:28
	ds_read2_b32 v[88:89], v79 offset0:32 offset1:36
	ds_read2_b32 v[90:91], v79 offset0:40 offset1:44
	ds_read2_b32 v[92:93], v79 offset0:48 offset1:52
	ds_read2_b32 v[94:95], v79 offset0:56 offset1:60
	v_lshlrev_b32_e32 v72, 3, v76
	v_lshl_or_b32 v72, v75, 2, v72
	v_cmp_gt_u32_e32 vcc, 2, v75
	s_waitcnt lgkmcnt(0)
	v_pk_mul_f32 v[96:97], v[80:81], v[0:1] op_sel_hi:[0,1]
	v_pk_mul_f32 v[98:99], v[80:81], v[2:3] op_sel_hi:[0,1]
	v_pk_mul_f32 v[100:101], v[80:81], v[4:5] op_sel:[1,0]
	v_pk_mul_f32 v[102:103], v[80:81], v[6:7] op_sel:[1,0]
	v_pk_fma_f32 v[96:97], v[82:83], v[8:9], v[96:97] op_sel_hi:[0,1,1]
	v_pk_fma_f32 v[98:99], v[82:83], v[10:11], v[98:99] op_sel_hi:[0,1,1]
	v_pk_fma_f32 v[100:101], v[82:83], v[12:13], v[100:101] op_sel:[1,0,0]
	v_pk_fma_f32 v[102:103], v[82:83], v[14:15], v[102:103] op_sel:[1,0,0]
	v_pk_fma_f32 v[96:97], v[84:85], v[16:17], v[96:97] op_sel_hi:[0,1,1]
	v_pk_fma_f32 v[98:99], v[84:85], v[18:19], v[98:99] op_sel_hi:[0,1,1]
	v_pk_fma_f32 v[100:101], v[84:85], v[20:21], v[100:101] op_sel:[1,0,0]
	v_pk_fma_f32 v[102:103], v[84:85], v[22:23], v[102:103] op_sel:[1,0,0]
	v_pk_fma_f32 v[96:97], v[86:87], v[24:25], v[96:97] op_sel_hi:[0,1,1]
	v_pk_fma_f32 v[98:99], v[86:87], v[26:27], v[98:99] op_sel_hi:[0,1,1]
	v_pk_fma_f32 v[100:101], v[86:87], v[28:29], v[100:101] op_sel:[1,0,0]
	v_pk_fma_f32 v[102:103], v[86:87], v[30:31], v[102:103] op_sel:[1,0,0]
	v_pk_fma_f32 v[96:97], v[88:89], v[32:33], v[96:97] op_sel_hi:[0,1,1]
	v_pk_fma_f32 v[98:99], v[88:89], v[34:35], v[98:99] op_sel_hi:[0,1,1]
	v_pk_fma_f32 v[100:101], v[88:89], v[36:37], v[100:101] op_sel:[1,0,0]
	v_pk_fma_f32 v[102:103], v[88:89], v[38:39], v[102:103] op_sel:[1,0,0]
	v_pk_fma_f32 v[96:97], v[90:91], v[40:41], v[96:97] op_sel_hi:[0,1,1]
	v_pk_fma_f32 v[98:99], v[90:91], v[42:43], v[98:99] op_sel_hi:[0,1,1]
	v_pk_fma_f32 v[100:101], v[90:91], v[44:45], v[100:101] op_sel:[1,0,0]
	v_pk_fma_f32 v[102:103], v[90:91], v[46:47], v[102:103] op_sel:[1,0,0]
	v_pk_fma_f32 v[96:97], v[92:93], v[48:49], v[96:97] op_sel_hi:[0,1,1]
	v_pk_fma_f32 v[98:99], v[92:93], v[50:51], v[98:99] op_sel_hi:[0,1,1]
	v_pk_fma_f32 v[100:101], v[92:93], v[52:53], v[100:101] op_sel:[1,0,0]
	v_pk_fma_f32 v[102:103], v[92:93], v[54:55], v[102:103] op_sel:[1,0,0]
	v_pk_fma_f32 v[96:97], v[94:95], v[56:57], v[96:97] op_sel_hi:[0,1,1]
	v_pk_fma_f32 v[98:99], v[94:95], v[58:59], v[98:99] op_sel_hi:[0,1,1]
	v_pk_fma_f32 v[100:101], v[94:95], v[60:61], v[100:101] op_sel:[1,0,0]
	v_pk_fma_f32 v[102:103], v[94:95], v[62:63], v[102:103] op_sel:[1,0,0]
	v_pk_add_f32 v[96:97], v[96:97], v[100:101]
	v_pk_add_f32 v[98:99], v[98:99], v[102:103]
	s_nop 1
	v_permlane16_swap_b32_e32 v96, v98
	v_permlane16_swap_b32_e32 v97, v99
	v_add_f32_e32 v96, v96, v98
	v_add_f32_e32 v97, v97, v99
	v_mov_b32_e32 v80, v96
	v_mov_b32_e32 v81, v97
	s_nop 1
	v_permlane32_swap_b32_e32 v96, v80
	v_permlane32_swap_b32_e32 v97, v81
	v_add_f32_e32 v96, v96, v80
	v_add_f32_e32 v97, v97, v81
	v_cvt_pk_f16_f32 v73, v96, v97
	s_and_saveexec_b64 s[4:5], vcc
	global_atomic_pk_add_f16 v72, v73, s[24:25]
	s_endpgm
	.p2align	8

_Z11edge_kernelILi64ELb0EEvPKfS1_PKDF16_PKiS5_S1_S1_S1_S1_S1_PDF16_:
	s_load_dwordx16 s[4:19], s[0:1], 0x10
	s_load_dwordx2 s[20:21], s[0:1], 0x50
	v_readfirstlane_b32 s3, v0
	v_bfe_u32 v75, v0, 4, 2
	v_and_b32_e32 v76, 15, v0
	v_and_b32_e32 v78, 63, v0
	s_lshr_b32 s3, s3, 6
	s_lshl_b32 s2, s2, 1
	s_add_i32 s2, s2, s3
	v_lshlrev_b32_e32 v74, 8, v75
	v_lshl_or_b32 v74, v76, 4, v74
	v_lshlrev_b32_e32 v79, 4, v78
	v_lshl_or_b32 v77, v76, 2, v75
	v_lshlrev_b32_e32 v77, 2, v77
	v_lshlrev_b32_e32 v78, 5, v75
	v_lshlrev_b32_e32 v73, 12, v75
	v_lshl_or_b32 v73, v76, 4, v73
	s_lshl_b32 s28, s2, 14
	s_lshl_b32 s29, s2, 14
	s_lshl_b32 s30, s2, 2
	s_lshl_b32 s31, s2, 8
	s_lshl_b32 s33, s3, 10
	s_lshl_b32 s34, s3, 8
	s_addk_i32 s34, 0x4000
	s_waitcnt lgkmcnt(0)
	s_add_u32 s6, s6, s30
	s_addc_u32 s7, s7, 0
	s_add_u32 s8, s8, s30
	s_addc_u32 s9, s9, 0
	s_load_dword s35, s[6:7], 0x0
	s_load_dword s36, s[8:9], 0x0
	s_add_u32 s10, s10, s28
	s_addc_u32 s11, s11, 0
	s_add_u32 s18, s18, s33
	s_addc_u32 s19, s19, 0
	s_add_u32 s14, s14, s29
	s_addc_u32 s15, s15, 0
	s_add_u32 s12, s12, s31
	s_addc_u32 s13, s13, 0
	s_add_u32 s16, s16, s31
	s_addc_u32 s17, s17, 0
	s_waitcnt lgkmcnt(0)
	s_lshl_b32 s36, s36, 7
	s_add_u32 s20, s20, s36
	s_addc_u32 s21, s21, 0
	s_lshl_b32 s37, s35, 7
	s_add_u32 s4, s4, s37
	s_addc_u32 s5, s5, 0
	global_load_dwordx4 v[64:67], v78, s[4:5] nt
	global_load_dwordx4 v[68:71], v78, s[4:5] offset:16 nt
	v_add_u32_e32 v78, s34, v77
	s_waitcnt vmcnt(0)
	v_cvt_f32_f16_e32 v80, v64
	v_cvt_f32_f16_sdwa v81, v64 dst_sel:DWORD dst_unused:UNUSED_PAD src0_sel:WORD_1
	v_cvt_f32_f16_e32 v82, v65
	v_cvt_f32_f16_sdwa v83, v65 dst_sel:DWORD dst_unused:UNUSED_PAD src0_sel:WORD_1
	v_cvt_f32_f16_e32 v84, v66
	v_cvt_f32_f16_sdwa v85, v66 dst_sel:DWORD dst_unused:UNUSED_PAD src0_sel:WORD_1
	v_cvt_f32_f16_e32 v86, v67
	v_cvt_f32_f16_sdwa v87, v67 dst_sel:DWORD dst_unused:UNUSED_PAD src0_sel:WORD_1
	v_cvt_f32_f16_e32 v88, v68
	v_cvt_f32_f16_sdwa v89, v68 dst_sel:DWORD dst_unused:UNUSED_PAD src0_sel:WORD_1
	v_cvt_f32_f16_e32 v90, v69
	v_cvt_f32_f16_sdwa v91, v69 dst_sel:DWORD dst_unused:UNUSED_PAD src0_sel:WORD_1
	v_cvt_f32_f16_e32 v92, v70
	v_cvt_f32_f16_sdwa v93, v70 dst_sel:DWORD dst_unused:UNUSED_PAD src0_sel:WORD_1
	v_cvt_f32_f16_e32 v94, v71
	v_cvt_f32_f16_sdwa v95, v71 dst_sel:DWORD dst_unused:UNUSED_PAD src0_sel:WORD_1
	v_max_f32_e32 v80, 0, v80
	v_max_f32_e32 v81, 0, v81
	v_max_f32_e32 v82, 0, v82
	v_max_f32_e32 v83, 0, v83
	v_max_f32_e32 v84, 0, v84
	v_max_f32_e32 v85, 0, v85
	v_max_f32_e32 v86, 0, v86
	v_max_f32_e32 v87, 0, v87
	v_max_f32_e32 v88, 0, v88
	v_max_f32_e32 v89, 0, v89
	v_max_f32_e32 v90, 0, v90
	v_max_f32_e32 v91, 0, v91
	v_max_f32_e32 v92, 0, v92
	v_max_f32_e32 v93, 0, v93
	v_max_f32_e32 v94, 0, v94
	v_max_f32_e32 v95, 0, v95
	v_cmp_neq_f32_e64 s[40:41], 0, v80
	v_cmp_neq_f32_e64 s[42:43], 0, v81
	v_cmp_neq_f32_e64 s[44:45], 0, v82
	v_cmp_neq_f32_e64 s[46:47], 0, v83
	v_cmp_neq_f32_e64 s[48:49], 0, v84
	v_cmp_neq_f32_e64 s[50:51], 0, v85
	v_cmp_neq_f32_e64 s[52:53], 0, v86
	v_cmp_neq_f32_e64 s[54:55], 0, v87
	v_cmp_neq_f32_e64 s[56:57], 0, v88
	v_cmp_neq_f32_e64 s[58:59], 0, v89
	v_cmp_neq_f32_e64 s[60:61], 0, v90
	v_cmp_neq_f32_e64 s[62:63], 0, v91
	v_cmp_neq_f32_e64 s[64:65], 0, v92
	v_cmp_neq_f32_e64 s[66:67], 0, v93
	v_cmp_neq_f32_e64 s[68:69], 0, v94
	v_cmp_neq_f32_e64 s[70:71], 0, v95
	v_lshlrev_b32_e32 v96, 12, v75
	v_lshl_or_b32 v96, v76, 4, v96
	s_mov_b64 exec, s[40:41]
	global_load_dwordx4 v[0:3], v96, s[10:11] nt
	s_mov_b64 exec, s[42:43]
	global_load_dwordx4 v[4:7], v96, s[10:11] offset:256 nt
	s_mov_b64 exec, s[44:45]
	global_load_dwordx4 v[8:11], v96, s[10:11] offset:512 nt
	s_mov_b64 exec, s[46:47]
	global_load_dwordx4 v[12:15], v96, s[10:11] offset:768 nt
	s_mov_b64 exec, s[48:49]
	global_load_dwordx4 v[16:19], v96, s[10:11] offset:1024 nt
	s_mov_b64 exec, s[50:51]
	global_load_dwordx4 v[20:23], v96, s[10:11] offset:1280 nt
	s_mov_b64 exec, s[52:53]
	global_load_dwordx4 v[24:27], v96, s[10:11] offset:1536 nt
	s_mov_b64 exec, s[54:55]
	global_load_dwordx4 v[28:31], v96, s[10:11] offset:1792 nt
	s_mov_b64 exec, s[56:57]
	global_load_dwordx4 v[32:35], v96, s[10:11] offset:2048 nt
	s_mov_b64 exec, s[58:59]
	global_load_dwordx4 v[36:39], v96, s[10:11] offset:2304 nt
	s_mov_b64 exec, s[60:61]
	global_load_dwordx4 v[40:43], v96, s[10:11] offset:2560 nt
	s_mov_b64 exec, s[62:63]
	global_load_dwordx4 v[44:47], v96, s[10:11] offset:2816 nt
	s_mov_b64 exec, s[64:65]
	global_load_dwordx4 v[48:51], v96, s[10:11] offset:3072 nt
	s_mov_b64 exec, s[66:67]
	global_load_dwordx4 v[52:55], v96, s[10:11] offset:3328 nt
	s_mov_b64 exec, s[68:69]
	global_load_dwordx4 v[56:59], v96, s[10:11] offset:3584 nt
	s_mov_b64 exec, s[70:71]
	global_load_dwordx4 v[60:63], v96, s[10:11] offset:3840 nt
	s_mov_b64 exec, -1
	s_mov_b32 m0, s33
	s_nop 0
	global_load_lds_dwordx4 v79, s[18:19]
	global_load_lds_dwordx4 v79, s[18:19] offset:2048
	s_add_u32 m0, m0, 0x1000
	s_add_u32 s18, s18, 0x1000
	s_addc_u32 s19, s19, 0
	global_load_lds_dwordx4 v79, s[18:19]
	global_load_lds_dwordx4 v79, s[18:19] offset:2048
	s_add_u32 m0, m0, 0x1000
	s_add_u32 s18, s18, 0x1000
	s_addc_u32 s19, s19, 0
	global_load_lds_dwordx4 v79, s[18:19]
	global_load_lds_dwordx4 v79, s[18:19] offset:2048
	s_add_u32 m0, m0, 0x1000
	s_add_u32 s18, s18, 0x1000
	s_addc_u32 s19, s19, 0
	global_load_lds_dwordx4 v79, s[18:19]
	global_load_lds_dwordx4 v79, s[18:19] offset:2048
	global_load_dword v72, v77, s[12:13] nt
	global_load_dword v73, v77, s[16:17] nt
	v_lshl_add_u32 v79, v75, 2, s34
	v_mov_b32_e32 v96, 0
	v_mov_b32_e32 v97, 0
	v_mov_b32_e32 v98, 0
	v_mov_b32_e32 v99, 0
	v_mov_b32_e32 v100, 0
	v_mov_b32_e32 v101, 0
	v_mov_b32_e32 v102, 0
	v_mov_b32_e32 v103, 0
	s_waitcnt vmcnt(22)
	s_mov_b64 exec, s[40:41]
	v_pk_fma_f32 v[96:97], v[80:81], v[0:1], v[96:97] op_sel_hi:[0,1,1]
	v_pk_fma_f32 v[98:99], v[80:81], v[2:3], v[98:99] op_sel_hi:[0,1,1]
	s_mov_b64 exec, s[42:43]
	v_pk_fma_f32 v[100:101], v[80:81], v[4:5], v[100:101] op_sel:[1,0,0]
	v_pk_fma_f32 v[102:103], v[80:81], v[6:7], v[102:103] op_sel:[1,0,0]
	s_mov_b64 exec, s[44:45]
	v_pk_fma_f32 v[96:97], v[82:83], v[8:9], v[96:97] op_sel_hi:[0,1,1]
	v_pk_fma_f32 v[98:99], v[82:83], v[10:11], v[98:99] op_sel_hi:[0,1,1]
	s_mov_b64 exec, s[46:47]
	v_pk_fma_f32 v[100:101], v[82:83], v[12:13], v[100:101] op_sel:[1,0,0]
	v_pk_fma_f32 v[102:103], v[82:83], v[14:15], v[102:103] op_sel:[1,0,0]
	s_waitcnt vmcnt(18)
	s_mov_b64 exec, s[48:49]
	v_pk_fma_f32 v[96:97], v[84:85], v[16:17], v[96:97] op_sel_hi:[0,1,1]
	v_pk_fma_f32 v[98:99], v[84:85], v[18:19], v[98:99] op_sel_hi:[0,1,1]
	s_mov_b64 exec, s[50:51]
	v_pk_fma_f32 v[100:101], v[84:85], v[20:21], v[100:101] op_sel:[1,0,0]
	v_pk_fma_f32 v[102:103], v[84:85], v[22:23], v[102:103] op_sel:[1,0,0]
	s_mov_b64 exec, s[52:53]
	v_pk_fma_f32 v[96:97], v[86:87], v[24:25], v[96:97] op_sel_hi:[0,1,1]
	v_pk_fma_f32 v[98:99], v[86:87], v[26:27], v[98:99] op_sel_hi:[0,1,1]
	s_mov_b64 exec, s[54:55]
	v_pk_fma_f32 v[100:101], v[86:87], v[28:29], v[100:101] op_sel:[1,0,0]
	v_pk_fma_f32 v[102:103], v[86:87], v[30:31], v[102:103] op_sel:[1,0,0]
	s_waitcnt vmcnt(14)
	s_mov_b64 exec, s[56:57]
	v_pk_fma_f32 v[96:97], v[88:89], v[32:33], v[96:97] op_sel_hi:[0,1,1]
	v_pk_fma_f32 v[98:99], v[88:89], v[34:35], v[98:99] op_sel_hi:[0,1,1]
	s_mov_b64 exec, s[58:59]
	v_pk_fma_f32 v[100:101], v[88:89], v[36:37], v[100:101] op_sel:[1,0,0]
	v_pk_fma_f32 v[102:103], v[88:89], v[38:39], v[102:103] op_sel:[1,0,0]
	s_mov_b64 exec, s[60:61]
	v_pk_fma_f32 v[96:97], v[90:91], v[40:41], v[96:97] op_sel_hi:[0,1,1]
	v_pk_fma_f32 v[98:99], v[90:91], v[42:43], v[98:99] op_sel_hi:[0,1,1]
	s_mov_b64 exec, s[62:63]
	v_pk_fma_f32 v[100:101], v[90:91], v[44:45], v[100:101] op_sel:[1,0,0]
	v_pk_fma_f32 v[102:103], v[90:91], v[46:47], v[102:103] op_sel:[1,0,0]
	s_waitcnt vmcnt(10)
	s_mov_b64 exec, s[64:65]
	v_pk_fma_f32 v[96:97], v[92:93], v[48:49], v[96:97] op_sel_hi:[0,1,1]
	v_pk_fma_f32 v[98:99], v[92:93], v[50:51], v[98:99] op_sel_hi:[0,1,1]
	s_mov_b64 exec, s[66:67]
	v_pk_fma_f32 v[100:101], v[92:93], v[52:53], v[100:101] op_sel:[1,0,0]
	v_pk_fma_f32 v[102:103], v[92:93], v[54:55], v[102:103] op_sel:[1,0,0]
	s_mov_b64 exec, s[68:69]
	v_pk_fma_f32 v[96:97], v[94:95], v[56:57], v[96:97] op_sel_hi:[0,1,1]
	v_pk_fma_f32 v[98:99], v[94:95], v[58:59], v[98:99] op_sel_hi:[0,1,1]
	s_mov_b64 exec, s[70:71]
	v_pk_fma_f32 v[100:101], v[94:95], v[60:61], v[100:101] op_sel:[1,0,0]
	v_pk_fma_f32 v[102:103], v[94:95], v[62:63], v[102:103] op_sel:[1,0,0]
	s_mov_b64 exec, -1
	s_waitcnt vmcnt(0)
	s_barrier
	v_pk_add_f32 v[96:97], v[96:97], v[100:101]
	v_pk_add_f32 v[98:99], v[98:99], v[102:103]
	s_nop 1
	v_permlane16_swap_b32_e32 v96, v97
	v_permlane16_swap_b32_e32 v98, v99
	v_add_f32_e32 v96, v96, v97
	v_add_f32_e32 v98, v98, v99
	s_nop 1
	v_permlane32_swap_b32_e32 v96, v98
	v_add_f32_e32 v96, v96, v98
	s_waitcnt vmcnt(1)
	v_add_f32_e32 v96, v96, v72
	v_max_f32_e32 v96, 0, v96
	ds_write_b32 v78, v96
	ds_read2_b32 v[80:81], v79 offset0:0 offset1:4
	ds_read2_b32 v[82:83], v79 offset0:8 offset1:12
	ds_read2_b32 v[84:85], v79 offset0:16 offset1:20
	ds_read2_b32 v[86:87], v79 offset0:24 offset1:28
	ds_read2_b32 v[88:89], v79 offset0:32 offset1:36
	ds_read2_b32 v[90:91], v79 offset0:40 offset1:44
	ds_read2_b32 v[92:93], v79 offset0:48 offset1:52
	ds_read2_b32 v[94:95], v79 offset0:56 offset1:60
	s_waitcnt lgkmcnt(0)
	v_cmp_neq_f32_e64 s[40:41], 0, v80
	v_cmp_neq_f32_e64 s[42:43], 0, v81
	v_cmp_neq_f32_e64 s[44:45], 0, v82
	v_cmp_neq_f32_e64 s[46:47], 0, v83
	v_cmp_neq_f32_e64 s[48:49], 0, v84
	v_cmp_neq_f32_e64 s[50:51], 0, v85
	v_cmp_neq_f32_e64 s[52:53], 0, v86
	v_cmp_neq_f32_e64 s[54:55], 0, v87
	v_cmp_neq_f32_e64 s[56:57], 0, v88
	v_cmp_neq_f32_e64 s[58:59], 0, v89
	v_cmp_neq_f32_e64 s[60:61], 0, v90
	v_cmp_neq_f32_e64 s[62:63], 0, v91
	v_cmp_neq_f32_e64 s[64:65], 0, v92
	v_cmp_neq_f32_e64 s[66:67], 0, v93
	v_cmp_neq_f32_e64 s[68:69], 0, v94
	v_cmp_neq_f32_e64 s[70:71], 0, v95
	s_mov_b64 exec, s[40:41]
	global_load_dwordx4 v[0:3], v74, s[14:15] nt
	s_mov_b64 exec, s[42:43]
	global_load_dwordx4 v[4:7], v74, s[14:15] offset:1024 nt
	s_mov_b64 exec, s[44:45]
	global_load_dwordx4 v[8:11], v74, s[14:15] offset:2048 nt
	s_mov_b64 exec, s[46:47]
	global_load_dwordx4 v[12:15], v74, s[14:15] offset:3072 nt
	s_add_u32 s14, s14, 0x1000
	s_addc_u32 s15, s15, 0
	s_mov_b64 exec, s[48:49]
	global_load_dwordx4 v[16:19], v74, s[14:15] nt
	s_mov_b64 exec, s[50:51]
	global_load_dwordx4 v[20:23], v74, s[14:15] offset:1024 nt
	s_mov_b64 exec, s[52:53]
	global_load_dwordx4 v[24:27], v74, s[14:15] offset:2048 nt
	s_mov_b64 exec, s[54:55]
	global_load_dwordx4 v[28:31], v74, s[14:15] offset:3072 nt
	s_add_u32 s14, s14, 0x1000
	s_addc_u32 s15, s15, 0
	s_mov_b64 exec, s[56:57]
	global_load_dwordx4 v[32:35], v74, s[14:15] nt
	s_mov_b64 exec, s[58:59]
	global_load_dwordx4 v[36:39], v74, s[14:15] offset:1024 nt
	s_mov_b64 exec, s[60:61]
	global_load_dwordx4 v[40:43], v74, s[14:15] offset:2048 nt
	s_mov_b64 exec, s[62:63]
	global_load_dwordx4 v[44:47], v74, s[14:15] offset:3072 nt
	s_add_u32 s14, s14, 0x1000
	s_addc_u32 s15, s15, 0
	s_mov_b64 exec, s[64:65]
	global_load_dwordx4 v[48:51], v74, s[14:15] nt
	s_mov_b64 exec, s[66:67]
	global_load_dwordx4 v[52:55], v74, s[14:15] offset:1024 nt
	s_mov_b64 exec, s[68:69]
	global_load_dwordx4 v[56:59], v74, s[14:15] offset:2048 nt
	s_mov_b64 exec, s[70:71]
	global_load_dwordx4 v[60:63], v74, s[14:15] offset:3072 nt
	s_mov_b64 exec, -1
	v_mov_b32_e32 v96, 0
	v_mov_b32_e32 v97, 0
	v_mov_b32_e32 v98, 0
	v_mov_b32_e32 v99, 0
	v_mov_b32_e32 v100, 0
	v_mov_b32_e32 v101, 0
	v_mov_b32_e32 v102, 0
	v_mov_b32_e32 v103, 0
	s_waitcnt vmcnt(12)
	s_mov_b64 exec, s[40:41]
	v_pk_fma_f32 v[96:97], v[80:81], v[0:1], v[96:97] op_sel_hi:[0,1,1]
	v_pk_fma_f32 v[98:99], v[80:81], v[2:3], v[98:99] op_sel_hi:[0,1,1]
	s_mov_b64 exec, s[42:43]
	v_pk_fma_f32 v[100:101], v[80:81], v[4:5], v[100:101] op_sel:[1,0,0]
	v_pk_fma_f32 v[102:103], v[80:81], v[6:7], v[102:103] op_sel:[1,0,0]
	s_mov_b64 exec, s[44:45]
	v_pk_fma_f32 v[96:97], v[82:83], v[8:9], v[96:97] op_sel_hi:[0,1,1]
	v_pk_fma_f32 v[98:99], v[82:83], v[10:11], v[98:99] op_sel_hi:[0,1,1]
	s_mov_b64 exec, s[46:47]
	v_pk_fma_f32 v[100:101], v[82:83], v[12:13], v[100:101] op_sel:[1,0,0]
	v_pk_fma_f32 v[102:103], v[82:83], v[14:15], v[102:103] op_sel:[1,0,0]
	s_waitcnt vmcnt(8)
	s_mov_b64 exec, s[48:49]
	v_pk_fma_f32 v[96:97], v[84:85], v[16:17], v[96:97] op_sel_hi:[0,1,1]
	v_pk_fma_f32 v[98:99], v[84:85], v[18:19], v[98:99] op_sel_hi:[0,1,1]
	s_mov_b64 exec, s[50:51]
	v_pk_fma_f32 v[100:101], v[84:85], v[20:21], v[100:101] op_sel:[1,0,0]
	v_pk_fma_f32 v[102:103], v[84:85], v[22:23], v[102:103] op_sel:[1,0,0]
	s_mov_b64 exec, s[52:53]
	v_pk_fma_f32 v[96:97], v[86:87], v[24:25], v[96:97] op_sel_hi:[0,1,1]
	v_pk_fma_f32 v[98:99], v[86:87], v[26:27], v[98:99] op_sel_hi:[0,1,1]
	s_mov_b64 exec, s[54:55]
	v_pk_fma_f32 v[100:101], v[86:87], v[28:29], v[100:101] op_sel:[1,0,0]
	v_pk_fma_f32 v[102:103], v[86:87], v[30:31], v[102:103] op_sel:[1,0,0]
	s_waitcnt vmcnt(4)
	s_mov_b64 exec, s[56:57]
	v_pk_fma_f32 v[96:97], v[88:89], v[32:33], v[96:97] op_sel_hi:[0,1,1]
	v_pk_fma_f32 v[98:99], v[88:89], v[34:35], v[98:99] op_sel_hi:[0,1,1]
	s_mov_b64 exec, s[58:59]
	v_pk_fma_f32 v[100:101], v[88:89], v[36:37], v[100:101] op_sel:[1,0,0]
	v_pk_fma_f32 v[102:103], v[88:89], v[38:39], v[102:103] op_sel:[1,0,0]
	s_mov_b64 exec, s[60:61]
	v_pk_fma_f32 v[96:97], v[90:91], v[40:41], v[96:97] op_sel_hi:[0,1,1]
	v_pk_fma_f32 v[98:99], v[90:91], v[42:43], v[98:99] op_sel_hi:[0,1,1]
	s_mov_b64 exec, s[62:63]
	v_pk_fma_f32 v[100:101], v[90:91], v[44:45], v[100:101] op_sel:[1,0,0]
	v_pk_fma_f32 v[102:103], v[90:91], v[46:47], v[102:103] op_sel:[1,0,0]
	s_waitcnt vmcnt(0)
	s_mov_b64 exec, s[64:65]
	v_pk_fma_f32 v[96:97], v[92:93], v[48:49], v[96:97] op_sel_hi:[0,1,1]
	v_pk_fma_f32 v[98:99], v[92:93], v[50:51], v[98:99] op_sel_hi:[0,1,1]
	s_mov_b64 exec, s[66:67]
	v_pk_fma_f32 v[100:101], v[92:93], v[52:53], v[100:101] op_sel:[1,0,0]
	v_pk_fma_f32 v[102:103], v[92:93], v[54:55], v[102:103] op_sel:[1,0,0]
	s_mov_b64 exec, s[68:69]
	v_pk_fma_f32 v[96:97], v[94:95], v[56:57], v[96:97] op_sel_hi:[0,1,1]
	v_pk_fma_f32 v[98:99], v[94:95], v[58:59], v[98:99] op_sel_hi:[0,1,1]
	s_mov_b64 exec, s[70:71]
	v_pk_fma_f32 v[100:101], v[94:95], v[60:61], v[100:101] op_sel:[1,0,0]
	v_pk_fma_f32 v[102:103], v[94:95], v[62:63], v[102:103] op_sel:[1,0,0]
	s_mov_b64 exec, -1
	ds_read_b128 v[0:3], v74
	ds_read_b128 v[4:7], v74 offset:1024
	ds_read_b128 v[8:11], v74 offset:2048
	ds_read_b128 v[12:15], v74 offset:3072
	ds_read_b128 v[16:19], v74 offset:4096
	ds_read_b128 v[20:23], v74 offset:5120
	ds_read_b128 v[24:27], v74 offset:6144
	ds_read_b128 v[28:31], v74 offset:7168
	ds_read_b128 v[32:35], v74 offset:8192
	ds_read_b128 v[36:39], v74 offset:9216
	ds_read_b128 v[40:43], v74 offset:10240
	ds_read_b128 v[44:47], v74 offset:11264
	ds_read_b128 v[48:51], v74 offset:12288
	ds_read_b128 v[52:55], v74 offset:13312
	ds_read_b128 v[56:59], v74 offset:14336
	v_pk_add_f32 v[96:97], v[96:97], v[100:101]
	v_pk_add_f32 v[98:99], v[98:99], v[102:103]
	s_nop 1
	v_permlane16_swap_b32_e32 v96, v97
	v_permlane16_swap_b32_e32 v98, v99
	v_add_f32_e32 v96, v96, v97
	v_add_f32_e32 v98, v98, v99
	s_nop 1
	v_permlane32_swap_b32_e32 v96, v98
	v_add_f32_e32 v96, v96, v98
	v_add_f32_e32 v96, v96, v73
	s_waitcnt lgkmcnt(5)
	ds_read_b128 v[60:63], v74 offset:15360
	ds_write_b32 v78, v96
	ds_read2_b32 v[80:81], v79 offset0:0 offset1:4
	ds_read2_b32 v[82:83], v79 offset0:8 offset1:12
	ds_read2_b32 v[84:85], v79 offset0:16 offset1:20
	ds_read2_b32 v[86:87], v79 offset0:24 offset1:28
	ds_read2_b32 v[88:89], v79 offset0:32 offset1:36
	ds_read2_b32 v[90:91], v79 offset0:40 offset1:44
	ds_read2_b32 v[92:93], v79 offset0:48 offset1:52
	ds_read2_b32 v[94:95], v79 offset0:56 offset1:60
	v_lshlrev_b32_e32 v72, 3, v76
	v_lshl_or_b32 v72, v75, 2, v72
	v_cmp_gt_u32_e32 vcc, 2, v75
	s_waitcnt lgkmcnt(0)
	v_pk_mul_f32 v[96:97], v[80:81], v[0:1] op_sel_hi:[0,1]
	v_pk_mul_f32 v[98:99], v[80:81], v[2:3] op_sel_hi:[0,1]
	v_pk_mul_f32 v[100:101], v[80:81], v[4:5] op_sel:[1,0]
	v_pk_mul_f32 v[102:103], v[80:81], v[6:7] op_sel:[1,0]
	v_pk_fma_f32 v[96:97], v[82:83], v[8:9], v[96:97] op_sel_hi:[0,1,1]
	v_pk_fma_f32 v[98:99], v[82:83], v[10:11], v[98:99] op_sel_hi:[0,1,1]
	v_pk_fma_f32 v[100:101], v[82:83], v[12:13], v[100:101] op_sel:[1,0,0]
	v_pk_fma_f32 v[102:103], v[82:83], v[14:15], v[102:103] op_sel:[1,0,0]
	v_pk_fma_f32 v[96:97], v[84:85], v[16:17], v[96:97] op_sel_hi:[0,1,1]
	v_pk_fma_f32 v[98:99], v[84:85], v[18:19], v[98:99] op_sel_hi:[0,1,1]
	v_pk_fma_f32 v[100:101], v[84:85], v[20:21], v[100:101] op_sel:[1,0,0]
	v_pk_fma_f32 v[102:103], v[84:85], v[22:23], v[102:103] op_sel:[1,0,0]
	v_pk_fma_f32 v[96:97], v[86:87], v[24:25], v[96:97] op_sel_hi:[0,1,1]
	v_pk_fma_f32 v[98:99], v[86:87], v[26:27], v[98:99] op_sel_hi:[0,1,1]
	v_pk_fma_f32 v[100:101], v[86:87], v[28:29], v[100:101] op_sel:[1,0,0]
	v_pk_fma_f32 v[102:103], v[86:87], v[30:31], v[102:103] op_sel:[1,0,0]
	v_pk_fma_f32 v[96:97], v[88:89], v[32:33], v[96:97] op_sel_hi:[0,1,1]
	v_pk_fma_f32 v[98:99], v[88:89], v[34:35], v[98:99] op_sel_hi:[0,1,1]
	v_pk_fma_f32 v[100:101], v[88:89], v[36:37], v[100:101] op_sel:[1,0,0]
	v_pk_fma_f32 v[102:103], v[88:89], v[38:39], v[102:103] op_sel:[1,0,0]
	v_pk_fma_f32 v[96:97], v[90:91], v[40:41], v[96:97] op_sel_hi:[0,1,1]
	v_pk_fma_f32 v[98:99], v[90:91], v[42:43], v[98:99] op_sel_hi:[0,1,1]
	v_pk_fma_f32 v[100:101], v[90:91], v[44:45], v[100:101] op_sel:[1,0,0]
	v_pk_fma_f32 v[102:103], v[90:91], v[46:47], v[102:103] op_sel:[1,0,0]
	v_pk_fma_f32 v[96:97], v[92:93], v[48:49], v[96:97] op_sel_hi:[0,1,1]
	v_pk_fma_f32 v[98:99], v[92:93], v[50:51], v[98:99] op_sel_hi:[0,1,1]
	v_pk_fma_f32 v[100:101], v[92:93], v[52:53], v[100:101] op_sel:[1,0,0]
	v_pk_fma_f32 v[102:103], v[92:93], v[54:55], v[102:103] op_sel:[1,0,0]
	v_pk_fma_f32 v[96:97], v[94:95], v[56:57], v[96:97] op_sel_hi:[0,1,1]
	v_pk_fma_f32 v[98:99], v[94:95], v[58:59], v[98:99] op_sel_hi:[0,1,1]
	v_pk_fma_f32 v[100:101], v[94:95], v[60:61], v[100:101] op_sel:[1,0,0]
	v_pk_fma_f32 v[102:103], v[94:95], v[62:63], v[102:103] op_sel:[1,0,0]
	v_pk_add_f32 v[96:97], v[96:97], v[100:101]
	v_pk_add_f32 v[98:99], v[98:99], v[102:103]
	s_nop 1
	v_permlane16_swap_b32_e32 v96, v98
	v_permlane16_swap_b32_e32 v97, v99
	v_add_f32_e32 v96, v96, v98
	v_add_f32_e32 v97, v97, v99
	v_mov_b32_e32 v80, v96
	v_mov_b32_e32 v81, v97
	s_nop 1
	v_permlane32_swap_b32_e32 v96, v80
	v_permlane32_swap_b32_e32 v97, v81
	v_add_f32_e32 v96, v96, v80
	v_add_f32_e32 v97, v97, v81
	v_cvt_pk_f16_f32 v73, v96, v97
	s_and_saveexec_b64 s[4:5], vcc
	global_atomic_pk_add_f16 v72, v73, s[20:21]
	s_endpgm
	.p2align	8
